# kernarg segment: the three later 64-byte lines touched next to the first s_load group (parallel cold misses instead of four serial ones)
# baseline (speedup 1.0000x reference)
_Z4mega5MArgs:
	s_load_dwordx4 s[28:31], s[0:1], 0xe0
	s_load_dword s33, s[0:1], 0xf0
	s_load_dword s99, s[0:1], 0x0
	s_load_dword s99, s[0:1], 0x40
	s_load_dword s99, s[0:1], 0x80
	s_add_u32 s4, s0, 0xf0
	s_addc_u32 s5, s1, 0
	v_lshrrev_b32_e32 v1, 6, v0
	s_nop 1
	v_readfirstlane_b32 s98, v1
	v_and_b32_e32 v1, 63, v0
	v_writelane_b32 v249, s4, 0
	v_cmp_eq_u32_e32 vcc, 0, v1
	s_nop 0
	v_writelane_b32 v249, s5, 1
	s_and_saveexec_b64 s[4:5], vcc
	s_cbranch_execz .LBB0_2
	s_getreg_b32 s3, hwreg(HW_REG_HW_ID, 0, 6)
	s_lshl_b32 s3, s3, 2
	s_and_b32 s3, s3, 0xfc
	s_add_i32 s3, s3, 0
	s_add_i32 s3, s3, 0x25c00
	v_lshrrev_b32_e32 v1, 6, v0
	v_mov_b32_e32 v2, s3
	ds_write_b32 v2, v1
